# E5b plus weight LDS reads hoisted under the previous pixel FMAs (LDS latency hiding)
# speedup vs baseline: 1.0053x; 1.0003x over previous
.Lwarm_skip:
	s_or_b64 exec, exec, s[10:11]
	v_mad_u64_u32 v[2:3], s[6:7], v71, 12, s[6:7]
	v_lshlrev_b32_e32 v4, 2, v71
	v_mov_b32_e32 v5, v69
	s_movk_i32 s6, 0xfe00
	v_lshl_add_u64 v[4:5], s[8:9], 0, v[4:5]
	v_lshl_add_u64 v[8:9], v[2:3], 0, v[6:7]
	s_mov_b32 s7, -1
	v_lshl_add_u64 v[4:5], v[4:5], 0, v[6:7]
	v_lshl_add_u64 v[2:3], v[8:9], 0, s[6:7]
	v_cmp_gt_u32_e32 vcc, 32, v1
	v_lshlrev_b32_e32 v33, 12, v10
	v_add_u32_e32 v34, v33, v6
	v_cndmask_b32_e32 v3, v3, v5, vcc
	v_cndmask_b32_e32 v2, v2, v4, vcc
	global_load_dwordx4 v[2:5], v[2:3], off
	v_and_b32_e32 v72, 1, v0
	v_lshl_add_u32 v0, v32, 4, v33
	v_lshlrev_b32_e32 v73, 4, v32
	v_lshlrev_b32_e32 v74, 6, v72
	v_xor_b32_e32 v73, v73, v74
	v_lshl_add_u32 v73, v72, 11, v73
	v_lshl_add_u32 v73, v10, 12, v73
	v_and_b32_e32 v74, 31, v1
	v_lshrrev_b32_e32 v75, 5, v1
	v_lshl_or_b32 v76, v74, 2, v71
	v_lshlrev_b32_e32 v74, 4, v74
	v_lshlrev_b32_e32 v77, 6, v75
	v_xor_b32_e32 v74, v74, v77
	v_lshl_add_u32 v74, v75, 11, v74
	v_lshl_add_u32 v74, v10, 12, v74
	v_lshlrev_b32_e32 v77, 7, v71
	v_and_b32_e32 v77, 0xe000000, v77
	v_and_b32_e32 v76, 0x3fffc, v76
	v_lshlrev_b32_e32 v75, 21, v75
	v_or3_b32 v75, v77, v75, v76
	v_lshlrev_b32_e32 v75, 2, v75
	s_mul_i32 s6, s4, 0x138800
	s_mul_hi_i32 s5, s4, 0x138800
	s_add_u32 s2, s2, s6
	s_addc_u32 s3, s3, s5
	global_load_dwordx4 v[28:31], v[8:9], off offset:512
	s_waitcnt vmcnt(1)
	ds_write_b128 v34, v[2:5]
	ds_read_b128 v[4:7], v0
	v_lshlrev_b32_e32 v0, 4, v72
	s_waitcnt lgkmcnt(0)
	v_max_i32_e32 v1, 0, v4
	v_max_i32_e32 v2, 0, v5
	v_max_i32_e32 v3, 0, v6
	v_max_i32_e32 v8, 0, v7
	v_lshl_or_b32 v35, v1, 7, v0
	v_lshl_or_b32 v36, v2, 7, v0
	v_lshl_or_b32 v37, v3, 7, v0
	v_lshl_or_b32 v38, v8, 7, v0
	global_load_dwordx4 v[20:23], v35, s[2:3]
	global_load_dwordx4 v[16:19], v35, s[2:3] offset:32
	global_load_dwordx4 v[8:11], v35, s[2:3] offset:64
	global_load_dwordx4 v[64:67], v36, s[2:3]
	global_load_dwordx4 v[60:63], v36, s[2:3] offset:32
	global_load_dwordx4 v[56:59], v36, s[2:3] offset:64
	global_load_dwordx4 v[52:55], v37, s[2:3]
	global_load_dwordx4 v[48:51], v37, s[2:3] offset:32
	global_load_dwordx4 v[44:47], v37, s[2:3] offset:64
	global_load_dwordx4 v[24:27], v38, s[2:3]
	global_load_dwordx4 v[12:15], v38, s[2:3] offset:32
	global_load_dwordx4 v[0:3], v38, s[2:3] offset:64
	s_waitcnt vmcnt(12)
	ds_write_b128 v34, v[28:31] offset:1024
	v_mul_u32_u24_e32 v28, 48, v32
	v_cmp_lt_i32_e32 vcc, -1, v4
	v_add_u32_e32 v31, v33, v28
	v_mov_b32_e32 v28, 0
	s_and_saveexec_b64 s[2:3], vcc
	ds_read_b32 v28, v31 offset:512
	s_or_b64 exec, exec, s[2:3]
	s_and_saveexec_b64 s[2:3], vcc
	ds_read_b32 v69, v31 offset:516
	s_or_b64 exec, exec, s[2:3]
	v_mov_b32_e32 v29, 0
	v_mov_b32_e32 v4, 0
	s_and_saveexec_b64 s[2:3], vcc
	ds_read_b32 v4, v31 offset:520
	s_or_b64 exec, exec, s[2:3]
	s_waitcnt vmcnt(11) lgkmcnt(0)
	v_fma_mix_f32 v30, v28, v20, v29 op_sel_hi:[0,1,0]
	v_fma_mix_f32 v20, v28, v20, v29 op_sel:[0,1,0] op_sel_hi:[0,1,0]
	v_fma_mix_f32 v32, v28, v21, v29 op_sel_hi:[0,1,0]
	v_fma_mix_f32 v21, v28, v21, v29 op_sel:[0,1,0] op_sel_hi:[0,1,0]
	v_fma_mix_f32 v33, v28, v22, v29 op_sel_hi:[0,1,0]
	v_fma_mix_f32 v22, v28, v22, v29 op_sel:[0,1,0] op_sel_hi:[0,1,0]
	v_fma_mix_f32 v34, v28, v23, v29 op_sel_hi:[0,1,0]
	v_fma_mix_f32 v23, v28, v23, v29 op_sel:[0,1,0] op_sel_hi:[0,1,0]
	s_waitcnt vmcnt(10)
	v_fma_mix_f32 v28, v69, v16, v30 op_sel_hi:[0,1,0]
	v_fma_mix_f32 v16, v69, v16, v20 op_sel:[0,1,0] op_sel_hi:[0,1,0]
	v_fma_mix_f32 v20, v69, v17, v32 op_sel_hi:[0,1,0]
	v_cmp_lt_i32_e32 vcc, -1, v5
	v_fma_mix_f32 v17, v69, v17, v21 op_sel:[0,1,0] op_sel_hi:[0,1,0]
	v_fma_mix_f32 v21, v69, v18, v33 op_sel_hi:[0,1,0]
	v_fma_mix_f32 v18, v69, v18, v22 op_sel:[0,1,0] op_sel_hi:[0,1,0]
	v_fma_mix_f32 v22, v69, v19, v34 op_sel_hi:[0,1,0]
	v_fma_mix_f32 v19, v69, v19, v23 op_sel:[0,1,0] op_sel_hi:[0,1,0]
	s_waitcnt vmcnt(9)
	s_and_saveexec_b64 s[2:3], vcc
	ds_read_b32 v29, v31 offset:524
	s_or_b64 exec, exec, s[2:3]
	v_mov_b32_e32 v5, 0
	s_and_saveexec_b64 s[2:3], vcc
	ds_read_b32 v5, v31 offset:532
	s_or_b64 exec, exec, s[2:3]
	v_fma_mix_f32 v40, v4, v8, v28 op_sel_hi:[0,1,0]
	v_fma_mix_f32 v36, v4, v8, v16 op_sel:[0,1,0] op_sel_hi:[0,1,0]
	v_fma_mix_f32 v32, v4, v9, v20 op_sel_hi:[0,1,0]
	v_fma_mix_f32 v28, v4, v9, v17 op_sel:[0,1,0] op_sel_hi:[0,1,0]
	v_mov_b32_e32 v9, 0
	s_and_saveexec_b64 s[2:3], vcc
	ds_read_b32 v9, v31 offset:528
	s_or_b64 exec, exec, s[2:3]
	v_fma_mix_f32 v20, v4, v10, v21 op_sel_hi:[0,1,0]
	v_fma_mix_f32 v16, v4, v10, v18 op_sel:[0,1,0] op_sel_hi:[0,1,0]
	v_fma_mix_f32 v8, v4, v11, v22 op_sel_hi:[0,1,0]
	v_fma_mix_f32 v4, v4, v11, v19 op_sel:[0,1,0] op_sel_hi:[0,1,0]
	v_mov_b32_e32 v10, 0
	s_waitcnt vmcnt(8) lgkmcnt(0)
	v_fma_mix_f32 v18, v29, v65, v10 op_sel_hi:[0,1,0]
	v_fma_mix_f32 v17, v29, v64, v10 op_sel:[0,1,0] op_sel_hi:[0,1,0]
	v_fma_mix_f32 v21, v29, v66, v10 op_sel_hi:[0,1,0]
	v_fma_mix_f32 v11, v29, v64, v10 op_sel_hi:[0,1,0]
	v_fma_mix_f32 v19, v29, v65, v10 op_sel:[0,1,0] op_sel_hi:[0,1,0]
	s_waitcnt vmcnt(7)
	v_fma_mix_f32 v18, v9, v61, v18 op_sel_hi:[0,1,0]
	v_fma_mix_f32 v22, v29, v66, v10 op_sel:[0,1,0] op_sel_hi:[0,1,0]
	v_fma_mix_f32 v23, v29, v67, v10 op_sel_hi:[0,1,0]
	v_fma_mix_f32 v29, v29, v67, v10 op_sel:[0,1,0] op_sel_hi:[0,1,0]
	v_fma_mix_f32 v17, v9, v60, v17 op_sel:[0,1,0] op_sel_hi:[0,1,0]
	v_fma_mix_f32 v21, v9, v62, v21 op_sel_hi:[0,1,0]
	s_waitcnt vmcnt(6)
	v_fma_mix_f32 v33, v5, v57, v18 op_sel_hi:[0,1,0]
	v_cmp_lt_i32_e32 vcc, -1, v6
	v_mov_b32_e32 v18, 0
	s_and_saveexec_b64 s[2:3], vcc
	ds_read_b32 v18, v31 offset:536
	s_or_b64 exec, exec, s[2:3]
	s_and_saveexec_b64 s[2:3], vcc
	ds_read_b32 v10, v31 offset:540
	s_or_b64 exec, exec, s[2:3]
	v_mov_b32_e32 v6, 0
	s_and_saveexec_b64 s[2:3], vcc
	ds_read_b32 v6, v31 offset:544
	s_or_b64 exec, exec, s[2:3]
	v_fma_mix_f32 v11, v9, v60, v11 op_sel_hi:[0,1,0]
	v_fma_mix_f32 v19, v9, v61, v19 op_sel:[0,1,0] op_sel_hi:[0,1,0]
	v_fma_mix_f32 v22, v9, v62, v22 op_sel:[0,1,0] op_sel_hi:[0,1,0]
	v_fma_mix_f32 v23, v9, v63, v23 op_sel_hi:[0,1,0]
	v_fma_mix_f32 v30, v9, v63, v29 op_sel:[0,1,0] op_sel_hi:[0,1,0]
	v_fma_mix_f32 v37, v5, v56, v17 op_sel:[0,1,0] op_sel_hi:[0,1,0]
	s_nop 0
	v_fma_mix_f32 v41, v5, v56, v11 op_sel_hi:[0,1,0]
	v_fma_mix_f32 v29, v5, v57, v19 op_sel:[0,1,0] op_sel_hi:[0,1,0]
	v_fma_mix_f32 v21, v5, v58, v21 op_sel_hi:[0,1,0]
	v_fma_mix_f32 v17, v5, v58, v22 op_sel:[0,1,0] op_sel_hi:[0,1,0]
	v_fma_mix_f32 v9, v5, v59, v23 op_sel_hi:[0,1,0]
	v_fma_mix_f32 v5, v5, v59, v30 op_sel:[0,1,0] op_sel_hi:[0,1,0]
	v_mov_b32_e32 v11, 0
	s_waitcnt vmcnt(5) lgkmcnt(0)
	v_fma_mix_f32 v22, v18, v52, v11 op_sel:[0,1,0] op_sel_hi:[0,1,0]
	v_fma_mix_f32 v30, v18, v53, v11 op_sel:[0,1,0] op_sel_hi:[0,1,0]
	v_fma_mix_f32 v19, v18, v52, v11 op_sel_hi:[0,1,0]
	v_fma_mix_f32 v23, v18, v53, v11 op_sel_hi:[0,1,0]
	v_fma_mix_f32 v34, v18, v54, v11 op_sel_hi:[0,1,0]
	v_fma_mix_f32 v35, v18, v54, v11 op_sel:[0,1,0] op_sel_hi:[0,1,0]
	v_fma_mix_f32 v38, v18, v55, v11 op_sel_hi:[0,1,0]
	v_fma_mix_f32 v18, v18, v55, v11 op_sel:[0,1,0] op_sel_hi:[0,1,0]
	s_waitcnt vmcnt(4)
	v_fma_mix_f32 v22, v10, v48, v22 op_sel:[0,1,0] op_sel_hi:[0,1,0]
	v_fma_mix_f32 v30, v10, v49, v30 op_sel:[0,1,0] op_sel_hi:[0,1,0]
	v_cmp_lt_i32_e32 vcc, -1, v7
	s_and_saveexec_b64 s[2:3], vcc
	ds_read_b32 v11, v31 offset:548
	s_or_b64 exec, exec, s[2:3]
	v_mov_b32_e32 v7, 0
	s_and_saveexec_b64 s[2:3], vcc
	ds_read_b32 v7, v31 offset:556
	s_or_b64 exec, exec, s[2:3]
	v_fma_mix_f32 v19, v10, v48, v19 op_sel_hi:[0,1,0]
	v_fma_mix_f32 v23, v10, v49, v23 op_sel_hi:[0,1,0]
	v_fma_mix_f32 v39, v10, v50, v34 op_sel_hi:[0,1,0]
	v_fma_mix_f32 v35, v10, v50, v35 op_sel:[0,1,0] op_sel_hi:[0,1,0]
	v_fma_mix_f32 v43, v10, v51, v38 op_sel_hi:[0,1,0]
	v_fma_mix_f32 v48, v10, v51, v18 op_sel:[0,1,0] op_sel_hi:[0,1,0]
	s_waitcnt vmcnt(3)
	v_fma_mix_f32 v42, v6, v44, v19 op_sel_hi:[0,1,0]
	v_mov_b32_e32 v19, 0
	s_and_saveexec_b64 s[2:3], vcc
	ds_read_b32 v19, v31 offset:552
	s_or_b64 exec, exec, s[2:3]
	v_fma_mix_f32 v38, v6, v44, v22 op_sel:[0,1,0] op_sel_hi:[0,1,0]
	v_fma_mix_f32 v34, v6, v45, v23 op_sel_hi:[0,1,0]
	v_fma_mix_f32 v30, v6, v45, v30 op_sel:[0,1,0] op_sel_hi:[0,1,0]
	v_fma_mix_f32 v22, v6, v46, v39 op_sel_hi:[0,1,0]
	v_fma_mix_f32 v18, v6, v46, v35 op_sel:[0,1,0] op_sel_hi:[0,1,0]
	v_fma_mix_f32 v10, v6, v47, v43 op_sel_hi:[0,1,0]
	v_fma_mix_f32 v6, v6, v47, v48 op_sel:[0,1,0] op_sel_hi:[0,1,0]
	s_load_dwordx2 s[0:1], s[0:1], 0x18
	s_ashr_i32 s5, s4, 31
	v_mov_b32_e32 v23, 0
	s_waitcnt vmcnt(2) lgkmcnt(0)
	v_fma_mix_f32 v31, v11, v24, v23 op_sel_hi:[0,1,0]
	v_fma_mix_f32 v24, v11, v24, v23 op_sel:[0,1,0] op_sel_hi:[0,1,0]
	v_fma_mix_f32 v35, v11, v25, v23 op_sel_hi:[0,1,0]
	v_fma_mix_f32 v25, v11, v25, v23 op_sel:[0,1,0] op_sel_hi:[0,1,0]
	v_fma_mix_f32 v39, v11, v26, v23 op_sel_hi:[0,1,0]
	v_fma_mix_f32 v26, v11, v26, v23 op_sel:[0,1,0] op_sel_hi:[0,1,0]
	v_fma_mix_f32 v43, v11, v27, v23 op_sel_hi:[0,1,0]
	v_fma_mix_f32 v11, v11, v27, v23 op_sel:[0,1,0] op_sel_hi:[0,1,0]
	s_waitcnt vmcnt(1)
	v_fma_mix_f32 v23, v19, v12, v31 op_sel_hi:[0,1,0]
	s_lshl_b64 s[2:3], s[4:5], 24
	v_fma_mix_f32 v12, v19, v12, v24 op_sel:[0,1,0] op_sel_hi:[0,1,0]
	v_fma_mix_f32 v24, v19, v13, v35 op_sel_hi:[0,1,0]
	v_fma_mix_f32 v13, v19, v13, v25 op_sel:[0,1,0] op_sel_hi:[0,1,0]
	v_fma_mix_f32 v25, v19, v14, v39 op_sel_hi:[0,1,0]
	v_fma_mix_f32 v14, v19, v14, v26 op_sel:[0,1,0] op_sel_hi:[0,1,0]
	v_fma_mix_f32 v26, v19, v15, v43 op_sel_hi:[0,1,0]
	v_fma_mix_f32 v15, v19, v15, v11 op_sel:[0,1,0] op_sel_hi:[0,1,0]
	s_add_u32 s0, s0, s2
	s_addc_u32 s1, s1, s3
	s_add_u32 s2, s0, 0x100000
	s_addc_u32 s3, s1, 0
	s_add_u32 s4, s0, 0x200000
	s_addc_u32 s5, s1, 0
	s_add_u32 s6, s0, 0x300000
	s_addc_u32 s7, s1, 0
	s_add_u32 s8, s0, 0x400000
	s_addc_u32 s9, s1, 0
	s_add_u32 s10, s0, 0x500000
	s_addc_u32 s11, s1, 0
	s_add_u32 s12, s0, 0x600000
	s_addc_u32 s13, s1, 0
	s_add_u32 s14, s0, 0x700000
	s_addc_u32 s15, s1, 0
	s_waitcnt vmcnt(0)
	v_fma_mix_f32 v43, v7, v0, v23 op_sel_hi:[0,1,0]
	v_fma_mix_f32 v23, v7, v2, v25 op_sel_hi:[0,1,0]
	v_fma_mix_f32 v19, v7, v2, v14 op_sel:[0,1,0] op_sel_hi:[0,1,0]
	v_fma_mix_f32 v39, v7, v0, v12 op_sel:[0,1,0] op_sel_hi:[0,1,0]
	v_fma_mix_f32 v35, v7, v1, v24 op_sel_hi:[0,1,0]
	v_fma_mix_f32 v31, v7, v1, v13 op_sel:[0,1,0] op_sel_hi:[0,1,0]
	v_fma_mix_f32 v11, v7, v3, v26 op_sel_hi:[0,1,0]
	v_fma_mix_f32 v7, v7, v3, v15 op_sel:[0,1,0] op_sel_hi:[0,1,0]
	ds_write_b128 v73, v[40:43]
	ds_write_b128 v73, v[36:39] offset:512
	ds_write_b128 v73, v[32:35] offset:1024
	ds_write_b128 v73, v[28:31] offset:1536
	ds_read_b128 v[44:47], v74
	ds_read_b128 v[48:51], v74 offset:512
	ds_read_b128 v[52:55], v74 offset:1024
	ds_read_b128 v[56:59], v74 offset:1536
	ds_write_b128 v73, v[20:23]
	ds_write_b128 v73, v[16:19] offset:512
	ds_write_b128 v73, v[8:11] offset:1024
	ds_write_b128 v73, v[4:7] offset:1536
	s_waitcnt lgkmcnt(7)
	global_store_dwordx4 v75, v[44:47], s[0:1] nt
	s_waitcnt lgkmcnt(6)
	global_store_dwordx4 v75, v[48:51], s[2:3] nt
	s_waitcnt lgkmcnt(5)
	global_store_dwordx4 v75, v[52:55], s[4:5] nt
	s_waitcnt lgkmcnt(4)
	global_store_dwordx4 v75, v[56:59], s[6:7] nt
	ds_read_b128 v[60:63], v74
	ds_read_b128 v[64:67], v74 offset:512
	ds_read_b128 v[0:3], v74 offset:1024
	ds_read_b128 v[12:15], v74 offset:1536
	s_waitcnt lgkmcnt(3)
	global_store_dwordx4 v75, v[60:63], s[8:9] nt
	s_waitcnt lgkmcnt(2)
	global_store_dwordx4 v75, v[64:67], s[10:11] nt
	s_waitcnt lgkmcnt(1)
	global_store_dwordx4 v75, v[0:3], s[12:13] nt
	s_waitcnt lgkmcnt(0)
	global_store_dwordx4 v75, v[12:15], s[14:15] nt
	s_endpgm
